# speedup vs baseline: 1.0007x; 1.0007x over previous
_Z11attn_kernelPK14__hip_bfloat16S1_S1_PS_:
	s_lshr_b32 s3, s2, 3
	s_and_b32 s33, s2, 7
	s_sub_i32 s4, 63, s3
	s_sub_i32 s3, s3, 32
	s_cmpk_lt_u32 s2, 0x100
	s_cselect_b32 s2, s4, s3
	v_lshrrev_b32_e32 v1, 6, v0
	s_ashr_i32 s77, s2, 1
	v_and_b32_e32 v184, 63, v0
	v_bfe_u32 v186, v0, 5, 1
	v_and_b32_e32 v185, 31, v0
	s_lshl_b32 s76, s2, 5
	v_cmp_ge_i32_e32 vcc, s77, v1
	v_mbcnt_lo_u32_b32 v50, -1, 0
	s_and_saveexec_b64 s[4:5], vcc
	s_xor_b64 s[70:71], exec, s[4:5]
	s_cbranch_execz .LBB2_8
	s_load_dwordx4 s[4:7], s[0:1], 0x0
	s_load_dwordx2 s[8:9], s[0:1], 0x10
	s_lshl_b32 s3, s33, 8
	s_lshl_b32 s2, s2, 2
	s_add_i32 s2, s2, s3
	s_ashr_i32 s3, s2, 31
	s_lshl_b64 s[2:3], s[2:3], 10
	s_waitcnt lgkmcnt(0)
	s_add_u32 s2, s4, s2
	s_addc_u32 s3, s5, s3
	s_lshl_b32 s10, s33, 18
	s_add_u32 s4, s6, s10
	s_addc_u32 s5, s7, 0
	s_add_u32 s6, s8, s10
	v_lshlrev_b32_e32 v34, 4, v184
	v_mov_b32_e32 v35, 0
	s_addc_u32 s7, s9, 0
	s_mov_b64 s[80:81], s[4:5]
	s_mov_b64 s[82:83], s[6:7]
	v_lshlrev_b32_e32 v203, 4, v184
	v_readfirstlane_b32 s78, v1
	global_load_dwordx4 v[68:71], v34, s[2:3]
	global_load_dwordx4 v[72:75], v34, s[2:3] offset:1024
	global_load_dwordx4 v[76:79], v34, s[2:3] offset:2048
	global_load_dwordx4 v[80:83], v34, s[2:3] offset:3072
	v_lshl_add_u64 v[180:181], s[4:5], 0, v[34:35]
	v_lshl_add_u64 v[182:183], s[6:7], 0, v[34:35]
	v_lshlrev_b32_e32 v34, 13, v1
	v_lshl_add_u64 v[2:3], v[180:181], 0, v[34:35]
	global_load_dwordx4 v[100:103], v[2:3], off
	global_load_dwordx4 v[108:111], v[2:3], off offset:1024
	global_load_dwordx4 v[116:119], v[2:3], off offset:2048
	global_load_dwordx4 v[120:123], v[2:3], off offset:3072
	v_or_b32_e32 v2, 0x1000, v34
	v_mov_b32_e32 v3, v35
	v_lshl_add_u64 v[4:5], v[180:181], 0, v[2:3]
	v_or_b32_e32 v6, 0x1400, v34
	v_mov_b32_e32 v7, v35
	v_lshl_add_u64 v[8:9], v[180:181], 0, v[6:7]
	global_load_dwordx4 v[132:135], v[4:5], off
	global_load_dwordx4 v[136:139], v[8:9], off
	v_or_b32_e32 v4, 0x1800, v34
	v_mov_b32_e32 v5, v35
	v_lshl_add_u64 v[8:9], v[180:181], 0, v[4:5]
	v_or_b32_e32 v10, 0x1c00, v34
	v_mov_b32_e32 v11, v35
	v_lshl_add_u64 v[12:13], v[180:181], 0, v[10:11]
	global_load_dwordx4 v[140:143], v[8:9], off
	global_load_dwordx4 v[144:147], v[12:13], off
	v_lshl_add_u64 v[8:9], v[182:183], 0, v[34:35]
	global_load_dwordx4 v[128:131], v[8:9], off
	global_load_dwordx4 v[124:127], v[8:9], off offset:1024
	global_load_dwordx4 v[112:115], v[8:9], off offset:2048
	global_load_dwordx4 v[104:107], v[8:9], off offset:3072
	v_lshl_add_u64 v[2:3], v[182:183], 0, v[2:3]
	v_lshl_add_u64 v[6:7], v[182:183], 0, v[6:7]
	global_load_dwordx4 v[84:87], v[2:3], off
	global_load_dwordx4 v[96:99], v[6:7], off
	v_lshl_add_u64 v[2:3], v[182:183], 0, v[4:5]
	v_lshl_add_u64 v[4:5], v[182:183], 0, v[10:11]
	global_load_dwordx4 v[88:91], v[2:3], off
	global_load_dwordx4 v[92:95], v[4:5], off
	v_lshlrev_b32_e32 v2, 2, v186
	v_lshl_or_b32 v2, s77, 6, v2
	v_or_b32_e32 v14, s76, v185
	v_or_b32_e32 v3, 32, v2
	v_cmp_gt_i32_e64 s[4:5], v3, v14
	v_or_b32_e32 v3, 33, v2
	v_cmp_gt_i32_e64 s[8:9], v3, v14
	v_or_b32_e32 v3, 2, v2
	v_cmp_gt_i32_e64 s[10:11], v3, v14
	v_or_b32_e32 v3, 34, v2
	v_cmp_gt_i32_e64 s[12:13], v3, v14
	v_or_b32_e32 v3, 3, v2
	v_cmp_gt_i32_e64 s[14:15], v3, v14
	v_or_b32_e32 v3, 35, v2
	v_cmp_gt_i32_e64 s[16:17], v3, v14
	v_or_b32_e32 v3, 8, v2
	v_cmp_gt_i32_e64 s[18:19], v3, v14
	v_or_b32_e32 v3, 40, v2
	v_cmp_gt_i32_e64 s[20:21], v3, v14
	v_or_b32_e32 v3, 9, v2
	v_cmp_gt_i32_e64 s[22:23], v3, v14
	v_or_b32_e32 v3, 41, v2
	v_cmp_gt_i32_e64 s[24:25], v3, v14
	v_or_b32_e32 v3, 10, v2
	v_cmp_gt_i32_e64 s[26:27], v3, v14
	v_or_b32_e32 v3, 42, v2
	v_cmp_gt_i32_e64 s[28:29], v3, v14
	v_or_b32_e32 v3, 11, v2
	v_cmp_gt_i32_e64 s[30:31], v3, v14
	v_or_b32_e32 v3, 43, v2
	v_cmp_gt_i32_e64 s[34:35], v3, v14
	v_or_b32_e32 v3, 16, v2
	v_cmp_gt_i32_e64 s[36:37], v3, v14
	v_or_b32_e32 v3, 48, v2
	v_cmp_gt_i32_e64 s[38:39], v3, v14
	v_or_b32_e32 v3, 17, v2
	v_cmp_gt_i32_e64 s[40:41], v3, v14
	v_or_b32_e32 v3, 49, v2
	v_cmp_gt_i32_e64 s[42:43], v3, v14
	v_or_b32_e32 v3, 18, v2
	v_cmp_gt_i32_e64 s[44:45], v3, v14
	v_or_b32_e32 v3, 50, v2
	v_cmp_gt_i32_e64 s[46:47], v3, v14
	v_or_b32_e32 v3, 19, v2
	v_cmp_gt_i32_e64 s[48:49], v3, v14
	v_or_b32_e32 v3, 51, v2
	v_cmp_gt_i32_e64 s[50:51], v3, v14
	v_or_b32_e32 v3, 24, v2
	v_cmp_gt_i32_e64 s[52:53], v3, v14
	v_or_b32_e32 v3, 56, v2
	v_cmp_gt_i32_e64 s[54:55], v3, v14
	v_or_b32_e32 v3, 25, v2
	v_cmp_gt_i32_e64 s[56:57], v3, v14
	v_or_b32_e32 v3, 57, v2
	v_cmp_gt_i32_e64 s[58:59], v3, v14
	v_or_b32_e32 v3, 26, v2
	v_cmp_gt_i32_e64 s[60:61], v3, v14
	v_or_b32_e32 v3, 58, v2
	v_cmp_gt_i32_e64 s[2:3], v2, v14
	v_cmp_lt_i32_e64 s[6:7], v2, v14
	v_cmp_gt_i32_e64 s[62:63], v3, v14
	v_or_b32_e32 v3, 27, v2
	v_or_b32_e32 v2, 59, v2
	v_mov_b32_e32 v34, v35
	v_cmp_gt_i32_e64 s[64:65], v3, v14
	v_cmp_gt_i32_e64 s[66:67], v2, v14
	v_mov_b32_e32 v36, v35
	v_mov_b32_e32 v37, v35
	v_mov_b32_e32 v38, v35
	v_mov_b32_e32 v39, v35
	v_mov_b32_e32 v40, v35
	v_mov_b32_e32 v41, v35
	v_mov_b32_e32 v42, v35
	v_mov_b32_e32 v43, v35
	v_mov_b32_e32 v44, v35
	v_mov_b32_e32 v45, v35
	v_mov_b32_e32 v46, v35
	v_mov_b32_e32 v47, v35
	v_mov_b32_e32 v48, v35
	v_mov_b32_e32 v49, v35
	v_mov_b64_e32 v[18:19], v[34:35]
	v_mov_b64_e32 v[2:3], v[34:35]
	v_mov_b32_e32 v190, 0xf149f2ca
	v_mov_b32_e32 v204, 0
	v_mov_b32_e32 v205, 0
	v_mov_b32_e32 v206, 0
	v_mov_b32_e32 v207, 0
	v_mov_b32_e32 v208, 0
	v_mov_b32_e32 v209, 0
	v_mov_b32_e32 v210, 0
	v_mov_b32_e32 v211, 0
	v_mov_b32_e32 v212, 0
	v_mov_b32_e32 v213, 0
	v_mov_b32_e32 v214, 0
	v_mov_b32_e32 v215, 0
	v_mov_b32_e32 v216, 0
	v_mov_b32_e32 v217, 0
	v_mov_b32_e32 v218, 0
	v_mov_b32_e32 v219, 0
	v_mov_b32_e32 v220, 0xff61b1e6
	v_mov_b32_e32 v221, 0xff61b1e6
	s_mov_b64 s[72:73], 0
	v_mbcnt_hi_u32_b32 v188, -1, v50
	v_mov_b32_e32 v187, 0
	v_mov_b64_e32 v[20:21], v[36:37]
	v_mov_b64_e32 v[22:23], v[38:39]
	v_mov_b64_e32 v[24:25], v[40:41]
	v_mov_b64_e32 v[26:27], v[42:43]
	v_mov_b64_e32 v[28:29], v[44:45]
	v_mov_b64_e32 v[30:31], v[46:47]
	v_mov_b64_e32 v[32:33], v[48:49]
	v_mov_b32_e32 v189, 0
	v_mov_b32_e32 v191, v1
	v_mov_b64_e32 v[4:5], v[36:37]
	v_mov_b64_e32 v[6:7], v[38:39]
	v_mov_b64_e32 v[8:9], v[40:41]
	v_mov_b64_e32 v[10:11], v[42:43]
	v_mov_b64_e32 v[12:13], v[44:45]
	v_mov_b64_e32 v[14:15], v[46:47]
	v_mov_b64_e32 v[16:17], v[48:49]
	s_branch .LBB2_3
.LBB2_2:
	v_exp_f32_e32 v197, v38
	v_exp_f32_e32 v198, v55
	v_exp_f32_e32 v194, v36
	v_exp_f32_e32 v196, v37
	v_exp_f32_e32 v199, v39
	v_exp_f32_e32 v40, v40
	v_exp_f32_e32 v36, v53
	v_exp_f32_e32 v37, v54
	v_exp_f32_e32 v38, v56
	v_exp_f32_e32 v39, v57
	v_exp_f32_e32 v41, v41
	v_exp_f32_e32 v193, v52
	v_add_f32_e32 v200, v36, v196
	v_add_f32_e32 v201, v37, v197
	v_pk_add_f32 v[52:53], v[38:39], v[40:41]
	v_exp_f32_e32 v54, v58
	v_exp_f32_e32 v55, v59
	v_cvt_pk_bf16_f32 v36, v193, v36
	v_cvt_pk_bf16_f32 v37, v37, v198
	v_cvt_pk_bf16_f32 v38, v38, v39
	v_cvt_pk_bf16_f32 v39, v54, v55
	s_waitcnt vmcnt(23)
	v_mfma_f32_32x32x16_bf16 v[18:33], v[128:131], v[36:39], v[18:33]
	v_exp_f32_e32 v56, v60
	s_waitcnt vmcnt(22)
	v_mfma_f32_32x32x16_bf16 v[2:17], v[124:127], v[36:39], v[2:17]
	v_exp_f32_e32 v57, v61
	v_exp_f32_e32 v58, v62
	v_exp_f32_e32 v59, v63
	v_exp_f32_e32 v60, v64
	v_exp_f32_e32 v61, v65
	v_exp_f32_e32 v62, v66
	v_exp_f32_e32 v63, v67
	v_cvt_pk_bf16_f32 v36, v56, v57
	v_cvt_pk_bf16_f32 v37, v58, v59
	v_cvt_pk_bf16_f32 v38, v60, v61
	v_cvt_pk_bf16_f32 v39, v62, v63
	s_waitcnt vmcnt(21)
	v_mfma_f32_32x32x16_bf16 v[18:33], v[112:115], v[36:39], v[18:33]
	v_exp_f32_e32 v44, v44
	v_exp_f32_e32 v45, v45
	v_add_f32_e32 v195, v193, v194
	v_pk_add_f32 v[56:57], v[56:57], v[44:45]
	s_waitcnt vmcnt(20)
	v_mfma_f32_32x32x16_bf16 v[2:17], v[104:107], v[36:39], v[2:17]
	v_cvt_pk_bf16_f32 v38, v40, v41
	v_cvt_pk_bf16_f32 v40, v44, v45
	v_add_f32_e32 v44, 0, v195
	v_exp_f32_e32 v42, v42
	v_exp_f32_e32 v43, v43
	v_exp_f32_e32 v51, v51
	v_cvt_pk_bf16_f32 v36, v194, v196
	v_cvt_pk_bf16_f32 v37, v197, v199
	v_cvt_pk_bf16_f32 v39, v42, v43
	v_add_f32_e32 v44, v44, v200
	s_waitcnt vmcnt(18)
	v_mfma_f32_32x32x16_bf16 v[2:17], v[96:99], v[36:39], v[2:17]
	v_add_f32_e32 v202, v198, v199
	v_add_f32_e32 v44, v44, v201
	v_add_f32_e32 v44, v44, v202
	v_add_f32_e32 v44, v44, v52
	v_exp_f32_e32 v46, v46
	v_mfma_f32_32x32x16_bf16 v[18:33], v[84:87], v[36:39], v[18:33]
	v_exp_f32_e32 v47, v47
	v_pk_add_f32 v[54:55], v[54:55], v[42:43]
	v_add_f32_e32 v44, v44, v53
	v_add_f32_e32 v44, v44, v54
	v_exp_f32_e32 v48, v48
	v_exp_f32_e32 v49, v49
	v_add_f32_e32 v44, v44, v55
	v_add_f32_e32 v44, v44, v56
	v_pk_add_f32 v[58:59], v[58:59], v[46:47]
	v_exp_f32_e32 v50, v50
	v_cvt_pk_bf16_f32 v41, v46, v47
	v_cvt_pk_bf16_f32 v42, v48, v49
	v_cvt_pk_bf16_f32 v43, v50, v51
	v_add_f32_e32 v36, v44, v57
	s_waitcnt vmcnt(16)
	v_mfma_f32_32x32x16_bf16 v[2:17], v[92:95], v[40:43], v[2:17]
	v_add_f32_e32 v36, v36, v58
	v_add_f32_e64 v60, v60, v48
	v_add_f32_e64 v61, v61, v49
	v_add_f32_e32 v36, v36, v59
	v_add_f32_e32 v36, v36, v60
	v_pk_add_f32 v[62:63], v[62:63], v[50:51]
	v_add_f32_e32 v36, v36, v61
	v_add_f32_e32 v36, v36, v62
	v_mfma_f32_32x32x16_bf16 v[18:33], v[88:91], v[40:43], v[18:33]
	s_and_b64 s[68:69], exec, s[68:69]
	v_add_f32_e32 v36, v36, v63
	s_waitcnt vmcnt(4)
	v_mov_b64_e32 v[104:105], v[168:169]
	v_mov_b64_e32 v[112:113], v[156:157]
	v_mov_b64_e32 v[124:125], v[152:153]
	v_mov_b64_e32 v[128:129], v[148:149]
	s_waitcnt vmcnt(3)
	v_mov_b64_e32 v[84:85], v[160:161]
	s_waitcnt vmcnt(2)
	v_mov_b64_e32 v[96:97], v[164:165]
	s_waitcnt vmcnt(1)
	v_mov_b64_e32 v[88:89], v[172:173]
	s_waitcnt vmcnt(0)
	v_mov_b64_e32 v[92:93], v[176:177]
	s_or_b64 s[72:73], s[68:69], s[72:73]
	v_add_f32_e32 v187, v187, v36
	v_mov_b64_e32 v[106:107], v[170:171]
	v_mov_b64_e32 v[114:115], v[158:159]
	v_mov_b64_e32 v[126:127], v[154:155]
	v_mov_b64_e32 v[130:131], v[150:151]
	v_mov_b64_e32 v[86:87], v[162:163]
	v_mov_b64_e32 v[98:99], v[166:167]
	v_mov_b64_e32 v[90:91], v[174:175]
	v_mov_b64_e32 v[94:95], v[178:179]
	s_andn2_b64 exec, exec, s[72:73]
	s_cbranch_execz .LBB2_7
.LBB2_3:
	s_add_u32 s79, s78, 4
	s_cmp_lt_i32 s77, s79
	s_cselect_b32 s79, s78, s79
	s_add_u32 s78, s78, 4
	s_lshl_b32 s79, s79, 13
	s_add_u32 s84, s80, s79
	s_addc_u32 s85, s81, 0
	s_add_u32 s86, s84, 0x1000
	s_addc_u32 s87, s85, 0
	s_add_u32 s88, s82, s79
	s_addc_u32 s89, s83, 0
	s_add_u32 s90, s88, 0x1000
	s_addc_u32 s91, s89, 0
	v_mov_b32_e32 v196, v191
	s_waitcnt vmcnt(9)
	v_mov_b64_e32 v[158:159], v[142:143]
	v_add_u32_e32 v191, 4, v196
	v_mfma_f32_32x32x16_bf16 v[52:67], v[100:103], v[68:71], v[204:219]
	v_mov_b64_e32 v[156:157], v[140:141]
	v_mov_b64_e32 v[142:143], v[138:139]
	v_cmp_lt_i32_e64 s[68:69], s77, v191
	v_mov_b64_e32 v[140:141], v[136:137]
	v_mov_b64_e32 v[138:139], v[110:111]
	v_mov_b64_e32 v[136:137], v[108:109]
	global_load_dwordx4 v[100:103], v203, s[84:85]
	global_load_dwordx4 v[108:111], v203, s[84:85] offset:1024
	v_mfma_f32_32x32x16_bf16 v[36:51], v[132:135], v[68:71], v[204:219]
	s_waitcnt vmcnt(10)
	v_mov_b64_e32 v[194:195], v[146:147]
	v_mov_b64_e32 v[192:193], v[144:145]
	v_mov_b64_e32 v[146:147], v[118:119]
	v_mov_b64_e32 v[144:145], v[116:117]
	v_mov_b64_e32 v[174:175], v[122:123]
	v_mov_b64_e32 v[172:173], v[120:121]
	v_mfma_f32_32x32x16_bf16 v[52:67], v[136:139], v[72:75], v[52:67]
	v_mfma_f32_32x32x16_bf16 v[36:51], v[140:143], v[72:75], v[36:51]
	v_mfma_f32_32x32x16_bf16 v[52:67], v[144:147], v[76:79], v[52:67]
	global_load_dwordx4 v[116:119], v203, s[84:85] offset:2048
	s_nop 0
	global_load_dwordx4 v[120:123], v203, s[84:85] offset:3072
	s_nop 0
	global_load_dwordx4 v[132:135], v203, s[86:87]
	s_nop 0
	global_load_dwordx4 v[136:139], v203, s[86:87] offset:1024
	s_nop 0
	global_load_dwordx4 v[140:143], v203, s[86:87] offset:2048
	s_nop 0
	global_load_dwordx4 v[144:147], v203, s[86:87] offset:3072
	global_load_dwordx4 v[148:151], v203, s[88:89]
	s_nop 0
	global_load_dwordx4 v[152:155], v203, s[88:89] offset:1024
	v_mfma_f32_32x32x16_bf16 v[36:51], v[156:159], v[76:79], v[36:51]
	global_load_dwordx4 v[156:159], v203, s[88:89] offset:2048
	global_load_dwordx4 v[168:171], v203, s[88:89] offset:3072
	global_load_dwordx4 v[160:163], v203, s[90:91]
	s_nop 0
	global_load_dwordx4 v[164:167], v203, s[90:91] offset:1024
	v_cmp_eq_u32_e32 vcc, s77, v196
	v_mfma_f32_32x32x16_bf16 v[52:67], v[172:175], v[80:83], v[52:67]
	global_load_dwordx4 v[172:175], v203, s[90:91] offset:2048
	s_nop 0
	global_load_dwordx4 v[176:179], v203, s[90:91] offset:3072
	v_mfma_f32_32x32x16_bf16 v[36:51], v[192:195], v[80:83], v[36:51]
	s_and_saveexec_b64 s[74:75], vcc
	s_cbranch_execz .LBB2_5
	s_nop 5
	v_cndmask_b32_e64 v34, v52, v190, s[2:3]
	s_nop 2
	v_cndmask_b32_e64 v36, v36, v190, s[4:5]
	v_cndmask_b32_e64 v53, v190, v53, s[6:7]
	v_cndmask_b32_e64 v52, v34, v52, s[6:7]
	v_cndmask_b32_e64 v37, v37, v190, s[8:9]
	v_cndmask_b32_e64 v54, v54, v190, s[10:11]
	v_cndmask_b32_e64 v38, v38, v190, s[12:13]
	v_cndmask_b32_e64 v55, v55, v190, s[14:15]
	v_cndmask_b32_e64 v39, v39, v190, s[16:17]
	v_cndmask_b32_e64 v56, v56, v190, s[18:19]
	v_cndmask_b32_e64 v40, v40, v190, s[20:21]
	v_cndmask_b32_e64 v57, v57, v190, s[22:23]
	v_cndmask_b32_e64 v41, v41, v190, s[24:25]
	v_cndmask_b32_e64 v58, v58, v190, s[26:27]
	v_cndmask_b32_e64 v42, v42, v190, s[28:29]
	v_cndmask_b32_e64 v59, v59, v190, s[30:31]
	v_cndmask_b32_e64 v43, v43, v190, s[34:35]
	v_cndmask_b32_e64 v60, v60, v190, s[36:37]
	v_cndmask_b32_e64 v44, v44, v190, s[38:39]
	v_cndmask_b32_e64 v61, v61, v190, s[40:41]
	v_cndmask_b32_e64 v45, v45, v190, s[42:43]
	v_cndmask_b32_e64 v62, v62, v190, s[44:45]
	v_cndmask_b32_e64 v46, v46, v190, s[46:47]
	v_cndmask_b32_e64 v63, v63, v190, s[48:49]
	v_cndmask_b32_e64 v47, v47, v190, s[50:51]
	v_cndmask_b32_e64 v64, v64, v190, s[52:53]
	v_cndmask_b32_e64 v48, v48, v190, s[54:55]
	v_cndmask_b32_e64 v65, v65, v190, s[56:57]
	v_cndmask_b32_e64 v49, v49, v190, s[58:59]
	v_cndmask_b32_e64 v66, v66, v190, s[60:61]
	v_cndmask_b32_e64 v50, v50, v190, s[62:63]
	v_cndmask_b32_e64 v67, v67, v190, s[64:65]
	v_cndmask_b32_e64 v51, v51, v190, s[66:67]
.LBB2_5:
	s_or_b64 exec, exec, s[74:75]
	s_nop 8
	v_max3_f32 v34, v52, v53, v54
	v_max3_f32 v192, v36, v37, v38
	v_max3_f32 v34, v34, v55, v56
	v_max3_f32 v192, v192, v39, v40
	v_max3_f32 v34, v34, v57, v58
	v_max3_f32 v192, v192, v41, v42
	v_max3_f32 v34, v34, v59, v60
	v_max3_f32 v192, v192, v43, v44
	v_max3_f32 v34, v34, v61, v62
	v_max3_f32 v192, v192, v45, v46
	v_max3_f32 v34, v34, v63, v64
	v_max3_f32 v192, v192, v47, v48
	v_max3_f32 v34, v34, v65, v66
	v_max3_f32 v192, v192, v49, v50
	v_max3_f32 v193, v34, v192, v67
	v_max_f32_e32 v193, v193, v51
	v_mov_b32_e32 v194, v193
	v_mov_b32_e32 v192, v193
	s_nop 1
	v_permlane32_swap_b32_e32 v194, v192
	v_max3_f32 v193, v193, v194, v192
	v_cmp_gt_f32_e32 vcc, v193, v220
	s_cbranch_vccz .LBB2_2
	v_max_f32_e32 v193, v193, v221
	v_mov_b32_e32 v220, 0x41000000
	v_mov_b32_e32 v221, 0
	v_add_f32_e32 v189, v189, v193
	v_min_f32_e64 v194, -v193, 0
	v_exp_f32_e32 v194, v194
	v_sub_f32_e32 v204, 0, v189
	v_sub_f32_e32 v36, v36, v193
	v_sub_f32_e32 v37, v37, v193
	v_sub_f32_e32 v38, v38, v193
	v_sub_f32_e32 v39, v39, v193
	v_sub_f32_e32 v40, v40, v193
	v_sub_f32_e32 v41, v41, v193
	v_sub_f32_e32 v42, v42, v193
	v_sub_f32_e32 v43, v43, v193
	v_sub_f32_e32 v44, v44, v193
	v_sub_f32_e32 v45, v45, v193
	v_sub_f32_e32 v46, v46, v193
	v_sub_f32_e32 v47, v47, v193
	v_sub_f32_e32 v48, v48, v193
	v_sub_f32_e32 v49, v49, v193
	v_sub_f32_e32 v50, v50, v193
	v_sub_f32_e32 v51, v51, v193
	v_sub_f32_e32 v52, v52, v193
	v_sub_f32_e32 v53, v53, v193
	v_sub_f32_e32 v54, v54, v193
	v_sub_f32_e32 v55, v55, v193
	v_sub_f32_e32 v56, v56, v193
	v_sub_f32_e32 v57, v57, v193
	v_sub_f32_e32 v58, v58, v193
	v_sub_f32_e32 v59, v59, v193
	v_sub_f32_e32 v60, v60, v193
	v_sub_f32_e32 v61, v61, v193
	v_sub_f32_e32 v62, v62, v193
	v_sub_f32_e32 v63, v63, v193
	v_sub_f32_e32 v64, v64, v193
	v_sub_f32_e32 v65, v65, v193
	v_sub_f32_e32 v66, v66, v193
	v_sub_f32_e32 v67, v67, v193
	v_mov_b32_e32 v205, v204
	v_mov_b32_e32 v206, v204
	v_mov_b32_e32 v207, v204
	v_mov_b32_e32 v208, v204
	v_mov_b32_e32 v209, v204
	v_mov_b32_e32 v210, v204
	v_mov_b32_e32 v211, v204
	v_mov_b32_e32 v212, v204
	v_mov_b32_e32 v213, v204
	v_mov_b32_e32 v214, v204
	v_mov_b32_e32 v215, v204
	v_mov_b32_e32 v216, v204
	v_mov_b32_e32 v217, v204
	v_mov_b32_e32 v218, v204
	v_mov_b32_e32 v219, v204
	v_pk_mul_f32 v[32:33], v[194:195], v[32:33] op_sel_hi:[0,1]
	v_pk_mul_f32 v[30:31], v[194:195], v[30:31] op_sel_hi:[0,1]
	v_pk_mul_f32 v[28:29], v[194:195], v[28:29] op_sel_hi:[0,1]
	v_pk_mul_f32 v[26:27], v[194:195], v[26:27] op_sel_hi:[0,1]
	v_pk_mul_f32 v[24:25], v[194:195], v[24:25] op_sel_hi:[0,1]
	v_pk_mul_f32 v[22:23], v[194:195], v[22:23] op_sel_hi:[0,1]
	v_pk_mul_f32 v[20:21], v[194:195], v[20:21] op_sel_hi:[0,1]
	v_pk_mul_f32 v[18:19], v[194:195], v[18:19] op_sel_hi:[0,1]
	v_pk_mul_f32 v[16:17], v[194:195], v[16:17] op_sel_hi:[0,1]
	v_pk_mul_f32 v[14:15], v[194:195], v[14:15] op_sel_hi:[0,1]
	v_pk_mul_f32 v[12:13], v[194:195], v[12:13] op_sel_hi:[0,1]
	v_pk_mul_f32 v[10:11], v[194:195], v[10:11] op_sel_hi:[0,1]
	v_pk_mul_f32 v[8:9], v[194:195], v[8:9] op_sel_hi:[0,1]
	v_pk_mul_f32 v[6:7], v[194:195], v[6:7] op_sel_hi:[0,1]
	v_pk_mul_f32 v[4:5], v[194:195], v[4:5] op_sel_hi:[0,1]
	v_pk_mul_f32 v[2:3], v[194:195], v[2:3] op_sel_hi:[0,1]
	v_mul_f32_e32 v187, v187, v194
	s_branch .LBB2_2

	.amdhsa_kernel _Z11attn_kernelPK14__hip_bfloat16S1_S1_PS_
		.amdhsa_group_segment_fixed_size 35840
		.amdhsa_private_segment_fixed_size 0
		.amdhsa_kernarg_size 32
		.amdhsa_user_sgpr_count 2
		.amdhsa_user_sgpr_dispatch_ptr 0
		.amdhsa_user_sgpr_queue_ptr 0
		.amdhsa_user_sgpr_kernarg_segment_ptr 1
		.amdhsa_user_sgpr_dispatch_id 0
		.amdhsa_user_sgpr_kernarg_preload_length 0
		.amdhsa_user_sgpr_kernarg_preload_offset 0
		.amdhsa_user_sgpr_private_segment_size 0
		.amdhsa_uses_dynamic_stack 0
		.amdhsa_enable_private_segment 0
		.amdhsa_system_sgpr_workgroup_id_x 1
		.amdhsa_system_sgpr_workgroup_id_y 0
		.amdhsa_system_sgpr_workgroup_id_z 0
		.amdhsa_system_sgpr_workgroup_info 0
		.amdhsa_system_vgpr_workitem_id 0
		.amdhsa_next_free_vgpr 224
		.amdhsa_next_free_sgpr 96
		.amdhsa_accum_offset 224
		.amdhsa_reserve_vcc 1
		.amdhsa_float_round_mode_32 0
		.amdhsa_float_round_mode_16_64 0
		.amdhsa_float_denorm_mode_32 3
		.amdhsa_float_denorm_mode_16_64 3
		.amdhsa_dx10_clamp 1
		.amdhsa_ieee_mode 1
		.amdhsa_fp16_overflow 0
		.amdhsa_tg_split 0
		.amdhsa_exception_fp_ieee_invalid_op 0
		.amdhsa_exception_fp_denorm_src 0
		.amdhsa_exception_fp_ieee_div_zero 0
		.amdhsa_exception_fp_ieee_overflow 0
		.amdhsa_exception_fp_ieee_underflow 0
		.amdhsa_exception_fp_ieee_inexact 0
		.amdhsa_exception_int_div_zero 0
	.end_amdhsa_kernel

amdhsa.kernels:
  - .agpr_count:     0
    .args:
      - .actual_access:  read_only
        .address_space:  global
        .offset:         0
        .size:           8
        .value_kind:     global_buffer
      - .actual_access:  read_only
        .address_space:  global
        .offset:         8
        .size:           8
        .value_kind:     global_buffer
      - .actual_access:  read_only
        .address_space:  global
        .offset:         16
        .size:           8
        .value_kind:     global_buffer
      - .actual_access:  read_only
        .address_space:  global
        .offset:         24
        .size:           8
        .value_kind:     global_buffer
      - .actual_access:  read_only
        .address_space:  global
        .offset:         32
        .size:           8
        .value_kind:     global_buffer
      - .actual_access:  read_only
        .address_space:  global
        .offset:         40
        .size:           8
        .value_kind:     global_buffer
      - .actual_access:  read_only
        .address_space:  global
        .offset:         48
        .size:           8
        .value_kind:     global_buffer
      - .actual_access:  write_only
        .address_space:  global
        .offset:         56
        .size:           8
        .value_kind:     global_buffer
      - .actual_access:  write_only
        .address_space:  global
        .offset:         64
        .size:           8
        .value_kind:     global_buffer
      - .actual_access:  write_only
        .address_space:  global
        .offset:         72
        .size:           8
        .value_kind:     global_buffer
    .group_segment_fixed_size: 0
    .kernarg_segment_align: 8
    .kernarg_segment_size: 80
    .language:       OpenCL C
    .language_version:
      - 2
      - 0
    .max_flat_workgroup_size: 256
    .name:           _Z11prep_kernelPKfS0_S0_S0_S0_S0_S0_PcS1_S1_
    .private_segment_fixed_size: 0
    .sgpr_count:     21
    .sgpr_spill_count: 0
    .symbol:         _Z11prep_kernelPKfS0_S0_S0_S0_S0_S0_PcS1_S1_.kd
    .uniform_work_group_size: 1
    .uses_dynamic_stack: false
    .vgpr_count:     52
    .vgpr_spill_count: 0
    .wavefront_size: 64
  - .agpr_count:     0
    .args:
      - .address_space:  global
        .offset:         0
        .size:           8
        .value_kind:     global_buffer
      - .address_space:  global
        .offset:         8
        .size:           8
        .value_kind:     global_buffer
      - .actual_access:  read_only
        .address_space:  global
        .offset:         16
        .size:           8
        .value_kind:     global_buffer
      - .actual_access:  read_only
        .address_space:  global
        .offset:         24
        .size:           8
        .value_kind:     global_buffer
      - .actual_access:  read_only
        .address_space:  global
        .offset:         32
        .size:           8
        .value_kind:     global_buffer
      - .actual_access:  write_only
        .address_space:  global
        .offset:         40
        .size:           8
        .value_kind:     global_buffer
      - .actual_access:  write_only
        .address_space:  global
        .offset:         48
        .size:           8
        .value_kind:     global_buffer
      - .actual_access:  write_only
        .address_space:  global
        .offset:         56
        .size:           8
        .value_kind:     global_buffer
      - .actual_access:  read_only
        .address_space:  global
        .offset:         64
        .size:           8
        .value_kind:     global_buffer
      - .actual_access:  write_only
        .address_space:  global
        .offset:         72
        .size:           8
        .value_kind:     global_buffer
    .group_segment_fixed_size: 131072
    .kernarg_segment_align: 8
    .kernarg_segment_size: 80
    .language:       OpenCL C
    .language_version:
      - 2
      - 0
    .max_flat_workgroup_size: 768
    .name:           _Z8qkv_gemmPKcS0_PKfS2_S2_P14__hip_bfloat16S4_S4_S2_Pc
    .private_segment_fixed_size: 0
    .sgpr_count:     106
    .sgpr_spill_count: 2
    .symbol:         _Z8qkv_gemmPKcS0_PKfS2_S2_P14__hip_bfloat16S4_S4_S2_Pc.kd
    .uniform_work_group_size: 1
    .uses_dynamic_stack: false
    .vgpr_count:     136
    .vgpr_spill_count: 0
    .wavefront_size: 64
  - .agpr_count:     0
    .args:
      - .address_space:  global
        .offset:         0
        .size:           8
        .value_kind:     global_buffer
      - .address_space:  global
        .offset:         8
        .size:           8
        .value_kind:     global_buffer
      - .address_space:  global
        .offset:         16
        .size:           8
        .value_kind:     global_buffer
      - .actual_access:  write_only
        .address_space:  global
        .offset:         24
        .size:           8
        .value_kind:     global_buffer
    .group_segment_fixed_size: 35840
    .kernarg_segment_align: 8
    .kernarg_segment_size: 32
    .language:       OpenCL C
    .language_version:
      - 2
      - 0
    .max_flat_workgroup_size: 256
    .name:           _Z11attn_kernelPK14__hip_bfloat16S1_S1_PS_
    .private_segment_fixed_size: 0
    .sgpr_count:     84
    .sgpr_spill_count: 0
    .symbol:         _Z11attn_kernelPK14__hip_bfloat16S1_S1_PS_.kd
    .uniform_work_group_size: 1
    .uses_dynamic_stack: false
    .vgpr_count:     224
    .vgpr_spill_count: 0
    .wavefront_size: 64
  - .agpr_count:     0
    .args:
      - .address_space:  global
        .offset:         0
        .size:           8
        .value_kind:     global_buffer
      - .address_space:  global
        .offset:         8
        .size:           8
        .value_kind:     global_buffer
      - .actual_access:  read_only
        .address_space:  global
        .offset:         16
        .size:           8
        .value_kind:     global_buffer
      - .actual_access:  read_only
        .address_space:  global
        .offset:         24
        .size:           8
        .value_kind:     global_buffer
      - .actual_access:  write_only
        .address_space:  global
        .offset:         32
        .size:           8
        .value_kind:     global_buffer
    .group_segment_fixed_size: 147456
    .kernarg_segment_align: 8
    .kernarg_segment_size: 40
    .language:       OpenCL C
    .language_version:
      - 2
      - 0
    .max_flat_workgroup_size: 512
    .name:           _Z7fc_gemmPKcS0_PKfS2_Pf
    .private_segment_fixed_size: 0
    .sgpr_count:     21
    .sgpr_spill_count: 0
    .symbol:         _Z7fc_gemmPKcS0_PKfS2_Pf.kd
    .uniform_work_group_size: 1
    .uses_dynamic_stack: false
    .vgpr_count:     192
    .vgpr_spill_count: 0
    .wavefront_size: 64
  - .agpr_count:     0
    .args:
      - .actual_access:  read_only
        .address_space:  global
        .offset:         0
        .size:           8
        .value_kind:     global_buffer
      - .actual_access:  write_only
        .address_space:  global
        .offset:         8
        .size:           8
        .value_kind:     global_buffer
      - .actual_access:  read_only
        .address_space:  global
        .offset:         16
        .size:           8
        .value_kind:     global_buffer
      - .actual_access:  read_only
        .address_space:  global
        .offset:         24
        .size:           8
        .value_kind:     global_buffer
    .group_segment_fixed_size: 16
    .kernarg_segment_align: 8
    .kernarg_segment_size: 32
    .language:       OpenCL C
    .language_version:
      - 2
      - 0
    .max_flat_workgroup_size: 256
    .name:           _Z9ln_kernelPKfPfS0_S0_
    .private_segment_fixed_size: 0
    .sgpr_count:     18
    .sgpr_spill_count: 0
    .symbol:         _Z9ln_kernelPKfPfS0_S0_.kd
    .uniform_work_group_size: 1
    .uses_dynamic_stack: false
    .vgpr_count:     74
    .vgpr_spill_count: 0
    .wavefront_size: 64
  - .agpr_count:     0
    .args:           []
    .group_segment_fixed_size: 0
    .kernarg_segment_align: 4
    .kernarg_segment_size: 0
    .language:       OpenCL C
    .language_version:
      - 2
      - 0
    .max_flat_workgroup_size: 1024
    .name:           _Z12empty_kernelv
    .private_segment_fixed_size: 0
    .sgpr_count:     6
    .sgpr_spill_count: 0
    .symbol:         _Z12empty_kernelv.kd
    .uniform_work_group_size: 1
    .uses_dynamic_stack: false
    .vgpr_count:     0
    .vgpr_spill_count: 0
    .wavefront_size: 64
